# v16 + P4 retention group-norm cross-row shuffles (xor16/xor32) via permlane swaps instead of ds_bpermute, both unit loops
# baseline (speedup 1.0000x reference)
.LBB0_629:
	ds_read_b128 v[206:209], v105
	ds_read_b128 v[210:213], v107
	s_waitcnt lgkmcnt(0)
	v_mfma_f32_16x16x32_bf16 v[94:97], v[210:213], v[206:209], v[94:97]
	ds_read_b128 v[210:213], v107 offset:4352
	s_waitcnt lgkmcnt(0)
	v_mfma_f32_16x16x32_bf16 v[90:93], v[210:213], v[206:209], v[90:93]
	ds_read_b128 v[210:213], v107 offset:8704
	s_waitcnt lgkmcnt(0)
	v_mfma_f32_16x16x32_bf16 v[86:89], v[210:213], v[206:209], v[86:89]
	ds_read_b128 v[210:213], v107 offset:13056
	s_waitcnt lgkmcnt(0)
	v_mfma_f32_16x16x32_bf16 v[82:85], v[210:213], v[206:209], v[82:85]
	ds_read_b128 v[210:213], v107 offset:17408
	s_waitcnt lgkmcnt(0)
	v_mfma_f32_16x16x32_bf16 v[78:81], v[210:213], v[206:209], v[78:81]
	ds_read_b128 v[210:213], v107 offset:21760
	s_waitcnt lgkmcnt(0)
	v_mfma_f32_16x16x32_bf16 v[74:77], v[210:213], v[206:209], v[74:77]
	ds_read_b128 v[210:213], v107 offset:26112
	s_waitcnt lgkmcnt(0)
	v_mfma_f32_16x16x32_bf16 v[70:73], v[210:213], v[206:209], v[70:73]
	ds_read_b128 v[210:213], v107 offset:30464
	s_waitcnt lgkmcnt(0)
	v_mfma_f32_16x16x32_bf16 v[66:69], v[210:213], v[206:209], v[66:69]
	s_add_i32 s3, s3, -1
	v_add_u32_e32 v107, 64, v107
	s_cmp_lg_u32 s3, 0
	v_add_u32_e32 v105, 64, v105
	s_cbranch_scc1 .LBB0_629
	ds_read_b128 v[206:209], v196
	ds_read_b128 v[210:213], v196 offset:4352
	ds_read_b128 v[214:217], v196 offset:8704
	ds_read_b128 v[218:221], v196 offset:13056
	ds_read_b128 v[222:225], v196 offset:17408
	ds_read_b128 v[226:229], v196 offset:21760
	ds_read_b128 v[230:233], v196 offset:26112
	ds_read_b128 v[234:237], v196 offset:30464
	s_waitcnt lgkmcnt(7)
	v_mfma_f32_16x16x32_bf16 v[206:209], v[206:209], v[62:65], 0
	s_waitcnt lgkmcnt(6)
	v_mfma_f32_16x16x32_bf16 v[210:213], v[210:213], v[62:65], 0
	s_waitcnt lgkmcnt(5)
	v_mfma_f32_16x16x32_bf16 v[214:217], v[214:217], v[62:65], 0
	s_waitcnt lgkmcnt(4)
	v_mfma_f32_16x16x32_bf16 v[218:221], v[218:221], v[62:65], 0
	s_waitcnt lgkmcnt(3)
	v_mfma_f32_16x16x32_bf16 v[222:225], v[222:225], v[62:65], 0
	s_waitcnt lgkmcnt(2)
	v_mfma_f32_16x16x32_bf16 v[226:229], v[226:229], v[62:65], 0
	s_waitcnt lgkmcnt(1)
	v_mfma_f32_16x16x32_bf16 v[230:233], v[230:233], v[62:65], 0
	s_waitcnt lgkmcnt(0)
	v_mfma_f32_16x16x32_bf16 v[62:65], v[234:237], v[62:65], 0
	ds_read_b128 v[234:237], v196 offset:64
	s_waitcnt lgkmcnt(0)
	v_mfma_f32_16x16x32_bf16 v[206:209], v[234:237], v[58:61], v[206:209]
	ds_read_b128 v[234:237], v196 offset:4416
	s_waitcnt lgkmcnt(0)
	v_mfma_f32_16x16x32_bf16 v[210:213], v[234:237], v[58:61], v[210:213]
	ds_read_b128 v[234:237], v196 offset:8768
	s_waitcnt lgkmcnt(0)
	v_mfma_f32_16x16x32_bf16 v[214:217], v[234:237], v[58:61], v[214:217]
	ds_read_b128 v[234:237], v196 offset:13120
	s_waitcnt lgkmcnt(0)
	v_mfma_f32_16x16x32_bf16 v[218:221], v[234:237], v[58:61], v[218:221]
	ds_read_b128 v[234:237], v196 offset:17472
	s_waitcnt lgkmcnt(0)
	v_mfma_f32_16x16x32_bf16 v[222:225], v[234:237], v[58:61], v[222:225]
	ds_read_b128 v[234:237], v196 offset:21824
	s_waitcnt lgkmcnt(0)
	v_mfma_f32_16x16x32_bf16 v[226:229], v[234:237], v[58:61], v[226:229]
	ds_read_b128 v[234:237], v196 offset:26176
	s_waitcnt lgkmcnt(0)
	v_mfma_f32_16x16x32_bf16 v[230:233], v[234:237], v[58:61], v[230:233]
	ds_read_b128 v[234:237], v196 offset:30528
	s_waitcnt lgkmcnt(0)
	v_mfma_f32_16x16x32_bf16 v[58:61], v[234:237], v[58:61], v[62:65]
	s_nop 2
	ds_read_b128 v[62:65], v196 offset:128
	s_waitcnt lgkmcnt(0)
	v_mfma_f32_16x16x32_bf16 v[62:65], v[62:65], v[54:57], v[206:209]
	s_nop 2
	ds_read_b128 v[206:209], v196 offset:4480
	s_waitcnt lgkmcnt(0)
	v_mfma_f32_16x16x32_bf16 v[206:209], v[206:209], v[54:57], v[210:213]
	s_nop 2
	ds_read_b128 v[210:213], v196 offset:8832
	s_waitcnt lgkmcnt(0)
	v_mfma_f32_16x16x32_bf16 v[210:213], v[210:213], v[54:57], v[214:217]
	s_nop 2
	ds_read_b128 v[214:217], v196 offset:13184
	s_waitcnt lgkmcnt(0)
	v_mfma_f32_16x16x32_bf16 v[214:217], v[214:217], v[54:57], v[218:221]
	s_nop 2
	ds_read_b128 v[218:221], v196 offset:17536
	s_waitcnt lgkmcnt(0)
	v_mfma_f32_16x16x32_bf16 v[218:221], v[218:221], v[54:57], v[222:225]
	s_nop 2
	ds_read_b128 v[222:225], v196 offset:21888
	s_waitcnt lgkmcnt(0)
	v_mfma_f32_16x16x32_bf16 v[222:225], v[222:225], v[54:57], v[226:229]
	s_nop 2
	ds_read_b128 v[226:229], v196 offset:26240
	s_waitcnt lgkmcnt(0)
	v_mfma_f32_16x16x32_bf16 v[226:229], v[226:229], v[54:57], v[230:233]
	s_nop 2
	ds_read_b128 v[230:233], v196 offset:30592
	s_waitcnt lgkmcnt(0)
	v_mfma_f32_16x16x32_bf16 v[54:57], v[230:233], v[54:57], v[58:61]
	s_nop 2
	ds_read_b128 v[58:61], v196 offset:192
	s_waitcnt lgkmcnt(0)
	v_mfma_f32_16x16x32_bf16 v[58:61], v[58:61], v[50:53], v[62:65]
	s_nop 2
	ds_read_b128 v[62:65], v196 offset:4544
	s_waitcnt lgkmcnt(0)
	v_mfma_f32_16x16x32_bf16 v[62:65], v[62:65], v[50:53], v[206:209]
	s_nop 2
	ds_read_b128 v[206:209], v196 offset:8896
	s_waitcnt lgkmcnt(0)
	v_mfma_f32_16x16x32_bf16 v[206:209], v[206:209], v[50:53], v[210:213]
	s_nop 2
	ds_read_b128 v[210:213], v196 offset:13248
	s_waitcnt lgkmcnt(0)
	v_mfma_f32_16x16x32_bf16 v[210:213], v[210:213], v[50:53], v[214:217]
	s_nop 2
	ds_read_b128 v[214:217], v196 offset:17600
	s_waitcnt lgkmcnt(0)
	v_mfma_f32_16x16x32_bf16 v[214:217], v[214:217], v[50:53], v[218:221]
	s_nop 2
	ds_read_b128 v[218:221], v196 offset:21952
	s_waitcnt lgkmcnt(0)
	v_mfma_f32_16x16x32_bf16 v[218:221], v[218:221], v[50:53], v[222:225]
	s_nop 2
	ds_read_b128 v[222:225], v196 offset:26304
	s_waitcnt lgkmcnt(0)
	v_mfma_f32_16x16x32_bf16 v[222:225], v[222:225], v[50:53], v[226:229]
	s_nop 2
	ds_read_b128 v[226:229], v196 offset:30656
	s_waitcnt lgkmcnt(0)
	v_mfma_f32_16x16x32_bf16 v[226:229], v[226:229], v[50:53], v[54:57]
	v_mul_f32_e32 v50, v103, v157
	v_cmp_gt_f32_e32 vcc, s89, v50
	s_mov_b32 s3, 0xf800000
	s_lshl_b32 s0, s0, 1
	v_cndmask_b32_e32 v51, 0, v200, vcc
	v_fmac_f32_e32 v51, v103, v157
	v_exp_f32_e32 v51, v51
	v_cndmask_b32_e32 v50, 0, v203, vcc
	v_ldexp_f32 v52, v51, v50
	v_pk_fma_f32 v[94:95], v[52:53], v[58:59], v[94:95] op_sel_hi:[0,1,1]
	v_pk_fma_f32 v[90:91], v[52:53], v[62:63], v[90:91] op_sel_hi:[0,1,1]
	v_pk_fma_f32 v[96:97], v[52:53], v[60:61], v[96:97] op_sel_hi:[0,1,1]
	v_pk_fma_f32 v[92:93], v[52:53], v[64:65], v[92:93] op_sel_hi:[0,1,1]
	v_mov_b32_e32 v50, v94
	v_mov_b32_e32 v51, v90
	v_mov_b32_e32 v54, v95
	v_mov_b32_e32 v55, v91
	v_pk_add_f32 v[50:51], v[50:51], v[54:55]
	v_mov_b32_e32 v54, v96
	v_mov_b32_e32 v55, v92
	v_mov_b32_e32 v56, v97
	v_mov_b32_e32 v57, v93
	v_pk_add_f32 v[54:55], v[54:55], v[56:57]
	v_pk_fma_f32 v[86:87], v[52:53], v[206:207], v[86:87] op_sel_hi:[0,1,1]
	v_pk_fma_f32 v[88:89], v[52:53], v[208:209], v[88:89] op_sel_hi:[0,1,1]
	v_pk_add_f32 v[50:51], v[50:51], v[54:55]
	v_pk_mov_b32 v[54:55], v[86:87], v[88:89] op_sel:[1,0]
	v_mov_b32_e32 v56, v86
	v_mov_b32_e32 v57, v89
	v_pk_add_f32 v[54:55], v[54:55], v[56:57]
	v_add_f32_e32 v50, 0, v50
	v_pk_add_f32 v[54:55], v[54:55], v[54:55] op_sel:[0,1] op_sel_hi:[1,0]
	v_pk_fma_f32 v[84:85], v[52:53], v[212:213], v[84:85] op_sel_hi:[0,1,1]
	v_pk_fma_f32 v[82:83], v[52:53], v[210:211], v[82:83] op_sel_hi:[0,1,1]
	v_pk_fma_f32 v[62:63], v[52:53], v[216:217], v[80:81] op_sel_hi:[0,1,1]
	v_pk_fma_f32 v[64:65], v[52:53], v[214:215], v[78:79] op_sel_hi:[0,1,1]
	v_add_f32_e32 v50, v50, v51
	v_add_f32_e32 v56, v82, v83
	v_add_f32_e32 v58, v84, v85
	v_mov_b32_e32 v51, v64
	v_mov_b32_e32 v55, v65
	v_mov_b32_e32 v57, v62
	v_mov_b32_e32 v59, v63
	v_pk_add_f32 v[50:51], v[50:51], v[54:55]
	v_pk_add_f32 v[54:55], v[56:57], v[58:59]
	v_pk_fma_f32 v[58:59], v[52:53], v[218:219], v[74:75] op_sel_hi:[0,1,1]
	v_pk_add_f32 v[50:51], v[50:51], v[54:55]
	v_pk_fma_f32 v[60:61], v[52:53], v[220:221], v[76:77] op_sel_hi:[0,1,1]
	v_pk_add_f32 v[78:79], v[50:51], v[50:51] op_sel:[0,1] op_sel_hi:[1,0]
	v_pk_mov_b32 v[50:51], v[58:59], v[60:61] op_sel:[1,0]
	v_mov_b32_e32 v54, v58
	v_mov_b32_e32 v55, v61
	v_pk_add_f32 v[50:51], v[50:51], v[54:55]
	v_pk_fma_f32 v[54:55], v[52:53], v[224:225], v[72:73] op_sel_hi:[0,1,1]
	v_pk_add_f32 v[74:75], v[50:51], v[50:51] op_sel:[0,1] op_sel_hi:[1,0]
	v_pk_fma_f32 v[56:57], v[52:53], v[222:223], v[70:71] op_sel_hi:[0,1,1]
	v_pk_fma_f32 v[50:51], v[52:53], v[228:229], v[68:69] op_sel_hi:[0,1,1]
	v_pk_fma_f32 v[52:53], v[52:53], v[226:227], v[66:67] op_sel_hi:[0,1,1]
	v_add_f32_e32 v70, v56, v57
	v_add_f32_e32 v72, v54, v55
	v_mov_b32_e32 v79, v52
	v_mov_b32_e32 v75, v53
	v_mov_b32_e32 v71, v50
	v_mov_b32_e32 v73, v51
	v_pk_add_f32 v[66:67], v[78:79], v[74:75]
	v_pk_add_f32 v[68:69], v[70:71], v[72:73]
	s_nop 0
	v_pk_add_f32 v[66:67], v[66:67], v[68:69]
	s_nop 0
	v_add_f32_e32 v66, v66, v67
	v_mov_b32_e32 v67, v66
	s_nop 1
	v_permlane16_swap_b32 v67, v66
	s_nop 0
	s_waitcnt lgkmcnt(0)
	v_add_f32_e32 v66, v66, v67
	v_mov_b32_e32 v67, v66
	s_nop 1
	v_permlane32_swap_b32 v67, v66
	s_nop 0
	s_waitcnt lgkmcnt(0)
	v_add_f32_e32 v103, v66, v67
	v_fmamk_f32 v70, v103, 0xbc000000, v97
	v_fmamk_f32 v72, v103, 0xbc000000, v95
	v_fmamk_f32 v71, v103, 0xbc000000, v93
	v_fmac_f32_e32 v92, 0xbc000000, v103
	v_fmamk_f32 v73, v103, 0xbc000000, v91
	v_fmac_f32_e32 v90, 0xbc000000, v103
	v_fmac_f32_e32 v96, 0xbc000000, v103
	v_fmac_f32_e32 v94, 0xbc000000, v103
	v_mov_b32_e32 v95, v90
	v_pk_mul_f32 v[66:67], v[72:73], v[72:73]
	v_mov_b32_e32 v97, v92
	v_pk_mul_f32 v[68:69], v[70:71], v[70:71]
	v_pk_fma_f32 v[66:67], v[94:95], v[94:95], v[66:67]
	v_pk_fma_f32 v[68:69], v[96:97], v[96:97], v[68:69]
	v_fmamk_f32 v87, v103, 0xbc000000, v87
	v_pk_add_f32 v[66:67], v[66:67], v[68:69]
	v_fmac_f32_e32 v86, 0xbc000000, v103
	v_fmamk_f32 v89, v103, 0xbc000000, v89
	v_fmac_f32_e32 v88, 0xbc000000, v103
	v_pk_add_f32 v[66:67], v[66:67], v[66:67] op_sel_hi:[0,1]
	v_pk_mul_f32 v[68:69], v[88:89], v[88:89]
	v_pk_mul_f32 v[74:75], v[86:87], v[86:87]
	v_fmac_f32_e32 v82, 0xbc000000, v103
	v_pk_mov_b32 v[76:77], v[74:75], v[68:69] op_sel:[1,0]
	v_mov_b32_e32 v75, v69
	v_fmamk_f32 v83, v103, 0xbc000000, v83
	v_fmac_f32_e32 v84, 0xbc000000, v103
	v_mul_f32_e32 v66, v82, v82
	v_pk_add_f32 v[68:69], v[76:77], v[74:75]
	v_fmamk_f32 v85, v103, 0xbc000000, v85
	v_pk_fma_f32 v[76:77], v[82:83], v[82:83], v[66:67] op_sel_hi:[1,1,0]
	v_mul_f32_e32 v66, v84, v84
	v_pk_add_f32 v[74:75], v[68:69], v[68:69] op_sel_hi:[0,1]
	v_pk_fma_f32 v[78:79], v[84:85], v[84:85], v[66:67] op_sel_hi:[1,1,0]
	v_fmamk_f32 v69, v103, 0xbc000000, v63
	v_fmac_f32_e32 v62, 0xbc000000, v103
	v_fmamk_f32 v68, v103, 0xbc000000, v65
	v_fmac_f32_e32 v64, 0xbc000000, v103
	v_mul_f32_e32 v76, v64, v64
	v_mul_f32_e32 v78, v68, v68
	v_mul_f32_e32 v74, v62, v62
	v_mul_f32_e32 v66, v69, v69
	v_pk_add_f32 v[76:77], v[76:77], v[78:79]
	v_pk_add_f32 v[66:67], v[74:75], v[66:67]
	v_fmamk_f32 v59, v103, 0xbc000000, v59
	v_pk_add_f32 v[66:67], v[76:77], v[66:67]
	v_fmac_f32_e32 v58, 0xbc000000, v103
	v_fmamk_f32 v61, v103, 0xbc000000, v61
	v_fmac_f32_e32 v60, 0xbc000000, v103
	v_pk_add_f32 v[74:75], v[66:67], v[66:67] op_sel_hi:[0,1]
	v_pk_mul_f32 v[66:67], v[60:61], v[60:61]
	v_pk_mul_f32 v[76:77], v[58:59], v[58:59]
	v_fmac_f32_e32 v56, 0xbc000000, v103
	v_pk_mov_b32 v[78:79], v[76:77], v[66:67] op_sel:[1,0]
	v_mov_b32_e32 v77, v67
	v_pk_add_f32 v[66:67], v[78:79], v[76:77]
	v_fmamk_f32 v57, v103, 0xbc000000, v57
	v_pk_add_f32 v[76:77], v[66:67], v[66:67] op_sel_hi:[0,1]
	v_fmac_f32_e32 v54, 0xbc000000, v103
	v_mul_f32_e32 v66, v56, v56
	v_fmamk_f32 v55, v103, 0xbc000000, v55
	v_pk_fma_f32 v[78:79], v[56:57], v[56:57], v[66:67] op_sel_hi:[1,1,0]
	v_mul_f32_e32 v66, v54, v54
	v_pk_fma_f32 v[80:81], v[54:55], v[54:55], v[66:67] op_sel_hi:[1,1,0]
	v_fmamk_f32 v67, v103, 0xbc000000, v51
	v_fmac_f32_e32 v50, 0xbc000000, v103
	v_fmamk_f32 v66, v103, 0xbc000000, v53
	v_fmac_f32_e32 v52, 0xbc000000, v103
	v_mul_f32_e32 v78, v52, v52
	v_mul_f32_e32 v80, v66, v66
	v_mul_f32_e32 v76, v50, v50
	v_mul_f32_e32 v74, v67, v67
	v_pk_add_f32 v[78:79], v[78:79], v[80:81]
	v_pk_add_f32 v[74:75], v[76:77], v[74:75]
	v_mov_b32_e32 v95, v96
	v_pk_add_f32 v[74:75], v[78:79], v[74:75]
	v_lshlrev_b32_e32 v81, 16, v145
	v_add_f32_e32 v51, v74, v75
	v_mov_b32_e32 v53, v51
	s_nop 1
	v_permlane16_swap_b32 v53, v51
	s_nop 0
	v_lshlrev_b32_e32 v80, 16, v144
	v_lshlrev_b64 v[76:77], 12, v[146:147]
	v_lshl_add_u64 v[76:77], s[90:91], 0, v[76:77]
	v_lshl_add_u64 v[76:77], v[76:77], 0, s[0:1]
	s_waitcnt lgkmcnt(0)
	v_add_f32_e32 v51, v51, v53
	v_mov_b32_e32 v53, v51
	s_nop 1
	v_permlane32_swap_b32 v53, v51
	s_nop 0
	v_lshl_add_u64 v[76:77], v[76:77], 0, v[98:99]
	v_mov_b32_e32 v91, v92
	s_waitcnt lgkmcnt(0)
	v_add_f32_e32 v51, v51, v53
	v_fmamk_f32 v51, v51, 0x3c000000, v197
	v_mul_f32_e32 v53, 0x4f800000, v51
	v_cmp_gt_f32_e32 vcc, s3, v51
	s_nop 1
	v_cndmask_b32_e32 v51, v51, v53, vcc
	v_sqrt_f32_e32 v53, v51
	s_nop 0
	v_add_u32_e32 v63, -1, v53
	v_fma_f32 v65, -v63, v53, v51
	v_cmp_ge_f32_e64 s[74:75], 0, v65
	v_add_u32_e32 v65, 1, v53
	s_nop 0
	v_cndmask_b32_e64 v63, v53, v63, s[74:75]
	v_fma_f32 v53, -v65, v53, v51
	v_cmp_lt_f32_e64 s[74:75], 0, v53
	s_nop 1
	v_cndmask_b32_e64 v53, v63, v65, s[74:75]
	v_mul_f32_e32 v63, 0x37800000, v53
	v_cndmask_b32_e32 v53, v53, v63, vcc
	v_cmp_class_f32_e32 vcc, v51, v199
	s_nop 1
	v_cndmask_b32_e32 v51, v53, v51, vcc
	v_div_scale_f32 v53, s[36:37], v51, v51, 1.0
	v_rcp_f32_e32 v63, v53
	s_nop 0
	v_fma_f32 v65, -v53, v63, 1.0
	v_fmac_f32_e32 v63, v65, v63
	v_div_scale_f32 v65, vcc, 1.0, v51, 1.0
	v_mul_f32_e32 v74, v65, v63
	v_fma_f32 v75, -v53, v74, v65
	v_fmac_f32_e32 v74, v75, v63
	v_fma_f32 v53, -v53, v74, v65
	v_div_fmas_f32 v53, v53, v63, v74
	v_div_fixup_f32 v74, v53, v51, 1.0
	v_pk_mul_f32 v[78:79], v[94:95], v[74:75] op_sel_hi:[1,0]
	v_and_b32_e32 v95, 0xffff0000, v145
	v_pk_mul_f32 v[78:79], v[78:79], v[80:81]
	v_mov_b32_e32 v80, v72
	v_mov_b32_e32 v81, v70
	v_pk_mul_f32 v[80:81], v[80:81], v[74:75] op_sel_hi:[1,0]
	v_and_b32_e32 v94, 0xffff0000, v144
	v_pk_mul_f32 v[80:81], v[80:81], v[94:95]
	v_and_b32_sdwa v51, v79, v204 dst_sel:DWORD dst_unused:UNUSED_PAD src0_sel:WORD_1 src1_sel:DWORD
	v_and_b32_sdwa v63, v81, v204 dst_sel:DWORD dst_unused:UNUSED_PAD src0_sel:WORD_1 src1_sel:DWORD
	v_and_b32_sdwa v65, v80, v204 dst_sel:DWORD dst_unused:UNUSED_PAD src0_sel:WORD_1 src1_sel:DWORD
	v_and_b32_sdwa v53, v78, v204 dst_sel:DWORD dst_unused:UNUSED_PAD src0_sel:WORD_1 src1_sel:DWORD
	v_add3_u32 v63, v81, v63, s34
	v_add3_u32 v65, v80, v65, s34
	v_add3_u32 v53, v78, v53, s34
	v_add3_u32 v51, v79, v51, s34
	v_and_b32_e32 v63, 0xffff0000, v63
	v_and_b32_e32 v65, 0xffff0000, v65
	v_mov_b32_e32 v70, v73
	v_or_b32_sdwa v79, v63, v51 dst_sel:DWORD dst_unused:UNUSED_PAD src0_sel:DWORD src1_sel:WORD_1
	v_or_b32_sdwa v78, v65, v53 dst_sel:DWORD dst_unused:UNUSED_PAD src0_sel:DWORD src1_sel:WORD_1
	v_pk_mul_f32 v[70:71], v[70:71], v[74:75] op_sel_hi:[1,0]
	v_and_b32_e32 v73, 0xffff0000, v143
	v_and_b32_e32 v72, 0xffff0000, v142
	global_store_dwordx2 v[76:77], v[78:79], off offset:2048
	v_pk_mul_f32 v[78:79], v[90:91], v[74:75] op_sel_hi:[1,0]
	v_lshlrev_b32_e32 v81, 16, v143
	v_lshlrev_b32_e32 v80, 16, v142
	v_pk_mul_f32 v[70:71], v[70:71], v[72:73]
	v_pk_mul_f32 v[78:79], v[78:79], v[80:81]
	v_and_b32_sdwa v63, v71, v204 dst_sel:DWORD dst_unused:UNUSED_PAD src0_sel:WORD_1 src1_sel:DWORD
	v_and_b32_sdwa v65, v70, v204 dst_sel:DWORD dst_unused:UNUSED_PAD src0_sel:WORD_1 src1_sel:DWORD
	v_and_b32_sdwa v51, v79, v204 dst_sel:DWORD dst_unused:UNUSED_PAD src0_sel:WORD_1 src1_sel:DWORD
	v_and_b32_sdwa v53, v78, v204 dst_sel:DWORD dst_unused:UNUSED_PAD src0_sel:WORD_1 src1_sel:DWORD
	v_add3_u32 v63, v71, v63, s34
	v_add3_u32 v65, v70, v65, s34
	v_add3_u32 v53, v78, v53, s34
	v_add3_u32 v51, v79, v51, s34
	v_and_b32_e32 v63, 0xffff0000, v63
	v_and_b32_e32 v65, 0xffff0000, v65
	v_or_b32_sdwa v71, v63, v51 dst_sel:DWORD dst_unused:UNUSED_PAD src0_sel:DWORD src1_sel:WORD_1
	v_or_b32_sdwa v70, v65, v53 dst_sel:DWORD dst_unused:UNUSED_PAD src0_sel:DWORD src1_sel:WORD_1
	global_store_dwordx2 v[76:77], v[70:71], off offset:2080
	v_mov_b32_e32 v70, v86
	v_mov_b32_e32 v71, v88
	v_pk_mul_f32 v[70:71], v[70:71], v[74:75] op_sel_hi:[1,0]
	v_lshlrev_b32_e32 v73, 16, v141
	v_lshlrev_b32_e32 v72, 16, v140
	v_mov_b32_e32 v88, v87
	v_pk_mul_f32 v[70:71], v[70:71], v[72:73]
	v_pk_mul_f32 v[72:73], v[88:89], v[74:75] op_sel_hi:[1,0]
	v_and_b32_e32 v79, 0xffff0000, v141
	v_and_b32_e32 v78, 0xffff0000, v140
	v_pk_mul_f32 v[72:73], v[72:73], v[78:79]
	v_and_b32_sdwa v51, v71, v204 dst_sel:DWORD dst_unused:UNUSED_PAD src0_sel:WORD_1 src1_sel:DWORD
	v_and_b32_sdwa v63, v73, v204 dst_sel:DWORD dst_unused:UNUSED_PAD src0_sel:WORD_1 src1_sel:DWORD
	v_and_b32_sdwa v65, v72, v204 dst_sel:DWORD dst_unused:UNUSED_PAD src0_sel:WORD_1 src1_sel:DWORD
	v_and_b32_sdwa v53, v70, v204 dst_sel:DWORD dst_unused:UNUSED_PAD src0_sel:WORD_1 src1_sel:DWORD
	v_add3_u32 v63, v73, v63, s34
	v_add3_u32 v65, v72, v65, s34
	v_add3_u32 v53, v70, v53, s34
	v_add3_u32 v51, v71, v51, s34
	v_and_b32_e32 v63, 0xffff0000, v63
	v_and_b32_e32 v65, 0xffff0000, v65
	v_or_b32_sdwa v71, v63, v51 dst_sel:DWORD dst_unused:UNUSED_PAD src0_sel:DWORD src1_sel:WORD_1
	v_or_b32_sdwa v70, v65, v53 dst_sel:DWORD dst_unused:UNUSED_PAD src0_sel:DWORD src1_sel:WORD_1
	global_store_dwordx2 v[76:77], v[70:71], off offset:2112
	v_mov_b32_e32 v70, v82
	v_mov_b32_e32 v71, v84
	v_pk_mul_f32 v[70:71], v[70:71], v[74:75] op_sel_hi:[1,0]
	v_lshlrev_b32_e32 v73, 16, v139
	v_lshlrev_b32_e32 v72, 16, v138
	v_mov_b32_e32 v84, v83
	v_pk_mul_f32 v[70:71], v[70:71], v[72:73]
	v_pk_mul_f32 v[72:73], v[84:85], v[74:75] op_sel_hi:[1,0]
	v_and_b32_e32 v79, 0xffff0000, v139
	v_and_b32_e32 v78, 0xffff0000, v138
	v_pk_mul_f32 v[72:73], v[72:73], v[78:79]
	v_and_b32_sdwa v53, v70, v204 dst_sel:DWORD dst_unused:UNUSED_PAD src0_sel:WORD_1 src1_sel:DWORD
	v_and_b32_sdwa v65, v72, v204 dst_sel:DWORD dst_unused:UNUSED_PAD src0_sel:WORD_1 src1_sel:DWORD
	v_and_b32_sdwa v63, v73, v204 dst_sel:DWORD dst_unused:UNUSED_PAD src0_sel:WORD_1 src1_sel:DWORD
	v_add3_u32 v65, v72, v65, s34
	v_and_b32_sdwa v51, v71, v204 dst_sel:DWORD dst_unused:UNUSED_PAD src0_sel:WORD_1 src1_sel:DWORD
	v_add3_u32 v53, v70, v53, s34
	v_add3_u32 v63, v73, v63, s34
	v_and_b32_e32 v65, 0xffff0000, v65
	v_add3_u32 v51, v71, v51, s34
	v_and_b32_e32 v63, 0xffff0000, v63
	v_or_b32_sdwa v70, v65, v53 dst_sel:DWORD dst_unused:UNUSED_PAD src0_sel:DWORD src1_sel:WORD_1
	v_mov_b32_e32 v65, v62
	v_or_b32_sdwa v71, v63, v51 dst_sel:DWORD dst_unused:UNUSED_PAD src0_sel:DWORD src1_sel:WORD_1
	v_pk_mul_f32 v[62:63], v[64:65], v[74:75] op_sel_hi:[1,0]
	v_lshlrev_b32_e32 v65, 16, v137
	v_lshlrev_b32_e32 v64, 16, v136
	v_pk_mul_f32 v[62:63], v[62:63], v[64:65]
	v_pk_mul_f32 v[64:65], v[68:69], v[74:75] op_sel_hi:[1,0]
	v_and_b32_e32 v69, 0xffff0000, v137
	v_and_b32_e32 v68, 0xffff0000, v136
	v_pk_mul_f32 v[64:65], v[64:65], v[68:69]
	v_and_b32_sdwa v51, v63, v204 dst_sel:DWORD dst_unused:UNUSED_PAD src0_sel:WORD_1 src1_sel:DWORD
	v_and_b32_sdwa v53, v62, v204 dst_sel:DWORD dst_unused:UNUSED_PAD src0_sel:WORD_1 src1_sel:DWORD
	v_add3_u32 v53, v62, v53, s34
	v_add3_u32 v51, v63, v51, s34
	v_and_b32_sdwa v62, v65, v204 dst_sel:DWORD dst_unused:UNUSED_PAD src0_sel:WORD_1 src1_sel:DWORD
	v_and_b32_sdwa v63, v64, v204 dst_sel:DWORD dst_unused:UNUSED_PAD src0_sel:WORD_1 src1_sel:DWORD
	v_add3_u32 v62, v65, v62, s34
	v_add3_u32 v63, v64, v63, s34
	v_and_b32_e32 v62, 0xffff0000, v62
	v_and_b32_e32 v64, 0xffff0000, v63
	v_or_b32_sdwa v63, v62, v51 dst_sel:DWORD dst_unused:UNUSED_PAD src0_sel:DWORD src1_sel:WORD_1
	v_or_b32_sdwa v62, v64, v53 dst_sel:DWORD dst_unused:UNUSED_PAD src0_sel:DWORD src1_sel:WORD_1
	global_store_dwordx2 v[76:77], v[62:63], off offset:2176
	v_mov_b32_e32 v63, v60
	v_mov_b32_e32 v60, v59
	v_mov_b32_e32 v62, v58
	v_pk_mul_f32 v[58:59], v[60:61], v[74:75] op_sel_hi:[1,0]
	v_and_b32_e32 v61, 0xffff0000, v135
	v_and_b32_e32 v60, 0xffff0000, v134
	v_pk_mul_f32 v[62:63], v[62:63], v[74:75] op_sel_hi:[1,0]
	v_lshlrev_b32_e32 v65, 16, v135
	v_lshlrev_b32_e32 v64, 16, v134
	v_pk_mul_f32 v[58:59], v[58:59], v[60:61]
	v_pk_mul_f32 v[62:63], v[62:63], v[64:65]
	v_and_b32_sdwa v60, v59, v204 dst_sel:DWORD dst_unused:UNUSED_PAD src0_sel:WORD_1 src1_sel:DWORD
	v_and_b32_sdwa v61, v58, v204 dst_sel:DWORD dst_unused:UNUSED_PAD src0_sel:WORD_1 src1_sel:DWORD
	v_and_b32_sdwa v51, v63, v204 dst_sel:DWORD dst_unused:UNUSED_PAD src0_sel:WORD_1 src1_sel:DWORD
	v_and_b32_sdwa v53, v62, v204 dst_sel:DWORD dst_unused:UNUSED_PAD src0_sel:WORD_1 src1_sel:DWORD
	v_add3_u32 v59, v59, v60, s34
	v_add3_u32 v58, v58, v61, s34
	v_add3_u32 v53, v62, v53, s34
	v_add3_u32 v51, v63, v51, s34
	v_and_b32_e32 v59, 0xffff0000, v59
	v_and_b32_e32 v58, 0xffff0000, v58
	v_or_b32_sdwa v59, v59, v51 dst_sel:DWORD dst_unused:UNUSED_PAD src0_sel:DWORD src1_sel:WORD_1
	v_or_b32_sdwa v58, v58, v53 dst_sel:DWORD dst_unused:UNUSED_PAD src0_sel:DWORD src1_sel:WORD_1
	global_store_dwordx2 v[76:77], v[58:59], off offset:2208
	v_mov_b32_e32 v59, v54
	v_mov_b32_e32 v54, v57
	v_mov_b32_e32 v58, v56
	v_pk_mul_f32 v[54:55], v[54:55], v[74:75] op_sel_hi:[1,0]
	v_and_b32_e32 v57, 0xffff0000, v133
	v_and_b32_e32 v56, 0xffff0000, v132
	v_pk_mul_f32 v[58:59], v[58:59], v[74:75] op_sel_hi:[1,0]
	v_lshlrev_b32_e32 v61, 16, v133
	v_lshlrev_b32_e32 v60, 16, v132
	v_pk_mul_f32 v[54:55], v[54:55], v[56:57]
	v_pk_mul_f32 v[58:59], v[58:59], v[60:61]
	v_and_b32_sdwa v57, v54, v204 dst_sel:DWORD dst_unused:UNUSED_PAD src0_sel:WORD_1 src1_sel:DWORD
	v_and_b32_sdwa v53, v58, v204 dst_sel:DWORD dst_unused:UNUSED_PAD src0_sel:WORD_1 src1_sel:DWORD
	v_and_b32_sdwa v56, v55, v204 dst_sel:DWORD dst_unused:UNUSED_PAD src0_sel:WORD_1 src1_sel:DWORD
	v_add3_u32 v54, v54, v57, s34
	v_and_b32_sdwa v51, v59, v204 dst_sel:DWORD dst_unused:UNUSED_PAD src0_sel:WORD_1 src1_sel:DWORD
	v_add3_u32 v53, v58, v53, s34
	v_add3_u32 v55, v55, v56, s34
	v_and_b32_e32 v54, 0xffff0000, v54
	v_add3_u32 v51, v59, v51, s34
	v_and_b32_e32 v55, 0xffff0000, v55
	v_or_b32_sdwa v54, v54, v53 dst_sel:DWORD dst_unused:UNUSED_PAD src0_sel:DWORD src1_sel:WORD_1
	v_mov_b32_e32 v53, v50
	v_or_b32_sdwa v55, v55, v51 dst_sel:DWORD dst_unused:UNUSED_PAD src0_sel:DWORD src1_sel:WORD_1
	v_pk_mul_f32 v[50:51], v[52:53], v[74:75] op_sel_hi:[1,0]
	v_lshlrev_b32_e32 v53, 16, v131
	v_lshlrev_b32_e32 v52, 16, v130
	global_store_dwordx2 v[76:77], v[54:55], off offset:2240
	v_pk_mul_f32 v[50:51], v[50:51], v[52:53]
	v_pk_mul_f32 v[52:53], v[66:67], v[74:75] op_sel_hi:[1,0]
	v_and_b32_e32 v55, 0xffff0000, v131
	v_and_b32_e32 v54, 0xffff0000, v130
	v_pk_mul_f32 v[52:53], v[52:53], v[54:55]
	v_and_b32_sdwa v54, v51, v204 dst_sel:DWORD dst_unused:UNUSED_PAD src0_sel:WORD_1 src1_sel:DWORD
	v_and_b32_sdwa v55, v50, v204 dst_sel:DWORD dst_unused:UNUSED_PAD src0_sel:WORD_1 src1_sel:DWORD
	v_add3_u32 v50, v50, v55, s34
	v_add3_u32 v51, v51, v54, s34
	v_and_b32_sdwa v54, v53, v204 dst_sel:DWORD dst_unused:UNUSED_PAD src0_sel:WORD_1 src1_sel:DWORD
	v_and_b32_sdwa v55, v52, v204 dst_sel:DWORD dst_unused:UNUSED_PAD src0_sel:WORD_1 src1_sel:DWORD
	v_add3_u32 v53, v53, v54, s34
	v_add3_u32 v52, v52, v55, s34
	v_and_b32_e32 v53, 0xffff0000, v53
	v_and_b32_e32 v52, 0xffff0000, v52
	v_or_b32_sdwa v51, v53, v51 dst_sel:DWORD dst_unused:UNUSED_PAD src0_sel:DWORD src1_sel:WORD_1
	v_or_b32_sdwa v50, v52, v50 dst_sel:DWORD dst_unused:UNUSED_PAD src0_sel:DWORD src1_sel:WORD_1
	global_store_dwordx2 v[76:77], v[50:51], off offset:2272
	s_waitcnt vmcnt(7)
	v_mov_b64_e32 v[64:65], v[36:37]
	v_mov_b64_e32 v[60:61], v[40:41]
	v_mov_b64_e32 v[56:57], v[44:45]
	v_mov_b64_e32 v[52:53], v[48:49]
	s_andn2_b64 vcc, exec, s[92:93]
	v_mov_b64_e32 v[62:63], v[34:35]
	v_mov_b64_e32 v[58:59], v[38:39]
	v_mov_b64_e32 v[54:55], v[42:43]
	v_mov_b64_e32 v[50:51], v[46:47]
	global_store_dwordx2 v[76:77], v[70:71], off offset:2144
	s_barrier
	s_cbranch_vccnz .LBB0_570

.LBB0_715:
	ds_read_b128 v[206:209], v105
	ds_read_b128 v[210:213], v107
	s_waitcnt lgkmcnt(0)
	v_mfma_f32_16x16x32_bf16 v[94:97], v[210:213], v[206:209], v[94:97]
	ds_read_b128 v[210:213], v107 offset:4352
	s_waitcnt lgkmcnt(0)
	v_mfma_f32_16x16x32_bf16 v[90:93], v[210:213], v[206:209], v[90:93]
	ds_read_b128 v[210:213], v107 offset:8704
	s_waitcnt lgkmcnt(0)
	v_mfma_f32_16x16x32_bf16 v[86:89], v[210:213], v[206:209], v[86:89]
	ds_read_b128 v[210:213], v107 offset:13056
	s_waitcnt lgkmcnt(0)
	v_mfma_f32_16x16x32_bf16 v[82:85], v[210:213], v[206:209], v[82:85]
	ds_read_b128 v[210:213], v107 offset:17408
	s_waitcnt lgkmcnt(0)
	v_mfma_f32_16x16x32_bf16 v[78:81], v[210:213], v[206:209], v[78:81]
	ds_read_b128 v[210:213], v107 offset:21760
	s_waitcnt lgkmcnt(0)
	v_mfma_f32_16x16x32_bf16 v[74:77], v[210:213], v[206:209], v[74:77]
	ds_read_b128 v[210:213], v107 offset:26112
	s_waitcnt lgkmcnt(0)
	v_mfma_f32_16x16x32_bf16 v[70:73], v[210:213], v[206:209], v[70:73]
	ds_read_b128 v[210:213], v107 offset:30464
	s_waitcnt lgkmcnt(0)
	v_mfma_f32_16x16x32_bf16 v[66:69], v[210:213], v[206:209], v[66:69]
	s_add_i32 s74, s74, -1
	v_add_u32_e32 v107, 64, v107
	s_cmp_lg_u32 s74, 0
	v_add_u32_e32 v105, 64, v105
	s_cbranch_scc1 .LBB0_715
	ds_read_b128 v[206:209], v194
	ds_read_b128 v[210:213], v194 offset:4352
	ds_read_b128 v[214:217], v194 offset:8704
	ds_read_b128 v[218:221], v194 offset:13056
	ds_read_b128 v[222:225], v194 offset:17408
	ds_read_b128 v[226:229], v194 offset:21760
	ds_read_b128 v[230:233], v194 offset:26112
	ds_read_b128 v[234:237], v194 offset:30464
	s_waitcnt lgkmcnt(7)
	v_mfma_f32_16x16x32_bf16 v[206:209], v[206:209], v[62:65], 0
	s_waitcnt lgkmcnt(6)
	v_mfma_f32_16x16x32_bf16 v[210:213], v[210:213], v[62:65], 0
	s_waitcnt lgkmcnt(5)
	v_mfma_f32_16x16x32_bf16 v[214:217], v[214:217], v[62:65], 0
	s_waitcnt lgkmcnt(4)
	v_mfma_f32_16x16x32_bf16 v[218:221], v[218:221], v[62:65], 0
	s_waitcnt lgkmcnt(3)
	v_mfma_f32_16x16x32_bf16 v[222:225], v[222:225], v[62:65], 0
	s_waitcnt lgkmcnt(2)
	v_mfma_f32_16x16x32_bf16 v[226:229], v[226:229], v[62:65], 0
	s_waitcnt lgkmcnt(1)
	v_mfma_f32_16x16x32_bf16 v[230:233], v[230:233], v[62:65], 0
	s_waitcnt lgkmcnt(0)
	v_mfma_f32_16x16x32_bf16 v[62:65], v[234:237], v[62:65], 0
	ds_read_b128 v[234:237], v194 offset:64
	s_waitcnt lgkmcnt(0)
	v_mfma_f32_16x16x32_bf16 v[206:209], v[234:237], v[58:61], v[206:209]
	ds_read_b128 v[234:237], v194 offset:4416
	s_waitcnt lgkmcnt(0)
	v_mfma_f32_16x16x32_bf16 v[210:213], v[234:237], v[58:61], v[210:213]
	ds_read_b128 v[234:237], v194 offset:8768
	s_waitcnt lgkmcnt(0)
	v_mfma_f32_16x16x32_bf16 v[214:217], v[234:237], v[58:61], v[214:217]
	ds_read_b128 v[234:237], v194 offset:13120
	s_waitcnt lgkmcnt(0)
	v_mfma_f32_16x16x32_bf16 v[218:221], v[234:237], v[58:61], v[218:221]
	ds_read_b128 v[234:237], v194 offset:17472
	s_waitcnt lgkmcnt(0)
	v_mfma_f32_16x16x32_bf16 v[222:225], v[234:237], v[58:61], v[222:225]
	ds_read_b128 v[234:237], v194 offset:21824
	s_waitcnt lgkmcnt(0)
	v_mfma_f32_16x16x32_bf16 v[226:229], v[234:237], v[58:61], v[226:229]
	ds_read_b128 v[234:237], v194 offset:26176
	s_waitcnt lgkmcnt(0)
	v_mfma_f32_16x16x32_bf16 v[230:233], v[234:237], v[58:61], v[230:233]
	ds_read_b128 v[234:237], v194 offset:30528
	s_waitcnt lgkmcnt(0)
	v_mfma_f32_16x16x32_bf16 v[58:61], v[234:237], v[58:61], v[62:65]
	s_nop 2
	ds_read_b128 v[62:65], v194 offset:128
	s_waitcnt lgkmcnt(0)
	v_mfma_f32_16x16x32_bf16 v[62:65], v[62:65], v[54:57], v[206:209]
	s_nop 2
	ds_read_b128 v[206:209], v194 offset:4480
	s_waitcnt lgkmcnt(0)
	v_mfma_f32_16x16x32_bf16 v[206:209], v[206:209], v[54:57], v[210:213]
	s_nop 2
	ds_read_b128 v[210:213], v194 offset:8832
	s_waitcnt lgkmcnt(0)
	v_mfma_f32_16x16x32_bf16 v[210:213], v[210:213], v[54:57], v[214:217]
	s_nop 2
	ds_read_b128 v[214:217], v194 offset:13184
	s_waitcnt lgkmcnt(0)
	v_mfma_f32_16x16x32_bf16 v[214:217], v[214:217], v[54:57], v[218:221]
	s_nop 2
	ds_read_b128 v[218:221], v194 offset:17536
	s_waitcnt lgkmcnt(0)
	v_mfma_f32_16x16x32_bf16 v[218:221], v[218:221], v[54:57], v[222:225]
	s_nop 2
	ds_read_b128 v[222:225], v194 offset:21888
	s_waitcnt lgkmcnt(0)
	v_mfma_f32_16x16x32_bf16 v[222:225], v[222:225], v[54:57], v[226:229]
	s_nop 2
	ds_read_b128 v[226:229], v194 offset:26240
	s_waitcnt lgkmcnt(0)
	v_mfma_f32_16x16x32_bf16 v[226:229], v[226:229], v[54:57], v[230:233]
	s_nop 2
	ds_read_b128 v[230:233], v194 offset:30592
	s_waitcnt lgkmcnt(0)
	v_mfma_f32_16x16x32_bf16 v[54:57], v[230:233], v[54:57], v[58:61]
	s_nop 2
	ds_read_b128 v[58:61], v194 offset:192
	s_waitcnt lgkmcnt(0)
	v_mfma_f32_16x16x32_bf16 v[58:61], v[58:61], v[50:53], v[62:65]
	s_nop 2
	ds_read_b128 v[62:65], v194 offset:4544
	s_waitcnt lgkmcnt(0)
	v_mfma_f32_16x16x32_bf16 v[62:65], v[62:65], v[50:53], v[206:209]
	s_nop 2
	ds_read_b128 v[206:209], v194 offset:8896
	s_waitcnt lgkmcnt(0)
	v_mfma_f32_16x16x32_bf16 v[206:209], v[206:209], v[50:53], v[210:213]
	s_nop 2
	ds_read_b128 v[210:213], v194 offset:13248
	s_waitcnt lgkmcnt(0)
	v_mfma_f32_16x16x32_bf16 v[210:213], v[210:213], v[50:53], v[214:217]
	s_nop 2
	ds_read_b128 v[214:217], v194 offset:17600
	s_waitcnt lgkmcnt(0)
	v_mfma_f32_16x16x32_bf16 v[214:217], v[214:217], v[50:53], v[218:221]
	s_nop 2
	ds_read_b128 v[218:221], v194 offset:21952
	s_waitcnt lgkmcnt(0)
	v_mfma_f32_16x16x32_bf16 v[218:221], v[218:221], v[50:53], v[222:225]
	s_nop 2
	ds_read_b128 v[222:225], v194 offset:26304
	s_waitcnt lgkmcnt(0)
	v_mfma_f32_16x16x32_bf16 v[222:225], v[222:225], v[50:53], v[226:229]
	s_nop 2
	ds_read_b128 v[226:229], v194 offset:30656
	s_waitcnt lgkmcnt(0)
	v_mfma_f32_16x16x32_bf16 v[226:229], v[226:229], v[50:53], v[54:57]
	v_mul_f32_e32 v50, v103, v157
	v_cmp_gt_f32_e32 vcc, s89, v50
	s_mov_b32 s34, 0xf800000
	s_lshl_b32 s0, s0, 1
	v_cndmask_b32_e32 v51, 0, v200, vcc
	v_fmac_f32_e32 v51, v103, v157
	v_exp_f32_e32 v51, v51
	v_cndmask_b32_e32 v50, 0, v203, vcc
	v_ldexp_f32 v52, v51, v50
	v_pk_fma_f32 v[94:95], v[52:53], v[58:59], v[94:95] op_sel_hi:[0,1,1]
	v_pk_fma_f32 v[90:91], v[52:53], v[62:63], v[90:91] op_sel_hi:[0,1,1]
	v_pk_fma_f32 v[96:97], v[52:53], v[60:61], v[96:97] op_sel_hi:[0,1,1]
	v_pk_fma_f32 v[92:93], v[52:53], v[64:65], v[92:93] op_sel_hi:[0,1,1]
	v_mov_b32_e32 v50, v94
	v_mov_b32_e32 v51, v90
	v_mov_b32_e32 v54, v95
	v_mov_b32_e32 v55, v91
	v_pk_add_f32 v[50:51], v[50:51], v[54:55]
	v_mov_b32_e32 v54, v96
	v_mov_b32_e32 v55, v92
	v_mov_b32_e32 v56, v97
	v_mov_b32_e32 v57, v93
	v_pk_add_f32 v[54:55], v[54:55], v[56:57]
	v_pk_fma_f32 v[86:87], v[52:53], v[206:207], v[86:87] op_sel_hi:[0,1,1]
	v_pk_fma_f32 v[88:89], v[52:53], v[208:209], v[88:89] op_sel_hi:[0,1,1]
	v_pk_add_f32 v[50:51], v[50:51], v[54:55]
	v_pk_mov_b32 v[54:55], v[86:87], v[88:89] op_sel:[1,0]
	v_mov_b32_e32 v56, v86
	v_mov_b32_e32 v57, v89
	v_pk_add_f32 v[54:55], v[54:55], v[56:57]
	v_add_f32_e32 v50, 0, v50
	v_pk_add_f32 v[54:55], v[54:55], v[54:55] op_sel:[0,1] op_sel_hi:[1,0]
	v_pk_fma_f32 v[84:85], v[52:53], v[212:213], v[84:85] op_sel_hi:[0,1,1]
	v_pk_fma_f32 v[82:83], v[52:53], v[210:211], v[82:83] op_sel_hi:[0,1,1]
	v_pk_fma_f32 v[62:63], v[52:53], v[216:217], v[80:81] op_sel_hi:[0,1,1]
	v_pk_fma_f32 v[64:65], v[52:53], v[214:215], v[78:79] op_sel_hi:[0,1,1]
	v_add_f32_e32 v50, v50, v51
	v_add_f32_e32 v56, v82, v83
	v_add_f32_e32 v58, v84, v85
	v_mov_b32_e32 v51, v64
	v_mov_b32_e32 v55, v65
	v_mov_b32_e32 v57, v62
	v_mov_b32_e32 v59, v63
	v_pk_add_f32 v[50:51], v[50:51], v[54:55]
	v_pk_add_f32 v[54:55], v[56:57], v[58:59]
	v_pk_fma_f32 v[58:59], v[52:53], v[218:219], v[74:75] op_sel_hi:[0,1,1]
	v_pk_add_f32 v[50:51], v[50:51], v[54:55]
	v_pk_fma_f32 v[60:61], v[52:53], v[220:221], v[76:77] op_sel_hi:[0,1,1]
	v_pk_add_f32 v[78:79], v[50:51], v[50:51] op_sel:[0,1] op_sel_hi:[1,0]
	v_pk_mov_b32 v[50:51], v[58:59], v[60:61] op_sel:[1,0]
	v_mov_b32_e32 v54, v58
	v_mov_b32_e32 v55, v61
	v_pk_add_f32 v[50:51], v[50:51], v[54:55]
	v_pk_fma_f32 v[54:55], v[52:53], v[224:225], v[72:73] op_sel_hi:[0,1,1]
	v_pk_add_f32 v[74:75], v[50:51], v[50:51] op_sel:[0,1] op_sel_hi:[1,0]
	v_pk_fma_f32 v[56:57], v[52:53], v[222:223], v[70:71] op_sel_hi:[0,1,1]
	v_pk_fma_f32 v[50:51], v[52:53], v[228:229], v[68:69] op_sel_hi:[0,1,1]
	v_pk_fma_f32 v[52:53], v[52:53], v[226:227], v[66:67] op_sel_hi:[0,1,1]
	v_add_f32_e32 v70, v56, v57
	v_add_f32_e32 v72, v54, v55
	v_mov_b32_e32 v79, v52
	v_mov_b32_e32 v75, v53
	v_mov_b32_e32 v71, v50
	v_mov_b32_e32 v73, v51
	v_pk_add_f32 v[66:67], v[78:79], v[74:75]
	v_pk_add_f32 v[68:69], v[70:71], v[72:73]
	s_nop 0
	v_pk_add_f32 v[66:67], v[66:67], v[68:69]
	s_nop 0
	v_add_f32_e32 v66, v66, v67
	v_mov_b32_e32 v67, v66
	s_nop 1
	v_permlane16_swap_b32 v67, v66
	s_nop 0
	s_waitcnt lgkmcnt(0)
	v_add_f32_e32 v66, v66, v67
	v_mov_b32_e32 v67, v66
	s_nop 1
	v_permlane32_swap_b32 v67, v66
	s_nop 0
	s_waitcnt lgkmcnt(0)
	v_add_f32_e32 v103, v66, v67
	v_fmamk_f32 v70, v103, 0xbc000000, v97
	v_fmamk_f32 v72, v103, 0xbc000000, v95
	v_fmamk_f32 v71, v103, 0xbc000000, v93
	v_fmac_f32_e32 v92, 0xbc000000, v103
	v_fmamk_f32 v73, v103, 0xbc000000, v91
	v_fmac_f32_e32 v90, 0xbc000000, v103
	v_fmac_f32_e32 v96, 0xbc000000, v103
	v_fmac_f32_e32 v94, 0xbc000000, v103
	v_mov_b32_e32 v95, v90
	v_pk_mul_f32 v[66:67], v[72:73], v[72:73]
	v_mov_b32_e32 v97, v92
	v_pk_mul_f32 v[68:69], v[70:71], v[70:71]
	v_pk_fma_f32 v[66:67], v[94:95], v[94:95], v[66:67]
	v_pk_fma_f32 v[68:69], v[96:97], v[96:97], v[68:69]
	v_fmamk_f32 v87, v103, 0xbc000000, v87
	v_pk_add_f32 v[66:67], v[66:67], v[68:69]
	v_fmac_f32_e32 v86, 0xbc000000, v103
	v_fmamk_f32 v89, v103, 0xbc000000, v89
	v_fmac_f32_e32 v88, 0xbc000000, v103
	v_pk_add_f32 v[66:67], v[66:67], v[66:67] op_sel_hi:[0,1]
	v_pk_mul_f32 v[68:69], v[88:89], v[88:89]
	v_pk_mul_f32 v[74:75], v[86:87], v[86:87]
	v_fmac_f32_e32 v82, 0xbc000000, v103
	v_pk_mov_b32 v[76:77], v[74:75], v[68:69] op_sel:[1,0]
	v_mov_b32_e32 v75, v69
	v_fmamk_f32 v83, v103, 0xbc000000, v83
	v_fmac_f32_e32 v84, 0xbc000000, v103
	v_mul_f32_e32 v66, v82, v82
	v_pk_add_f32 v[68:69], v[76:77], v[74:75]
	v_fmamk_f32 v85, v103, 0xbc000000, v85
	v_pk_fma_f32 v[76:77], v[82:83], v[82:83], v[66:67] op_sel_hi:[1,1,0]
	v_mul_f32_e32 v66, v84, v84
	v_pk_add_f32 v[74:75], v[68:69], v[68:69] op_sel_hi:[0,1]
	v_pk_fma_f32 v[78:79], v[84:85], v[84:85], v[66:67] op_sel_hi:[1,1,0]
	v_fmamk_f32 v69, v103, 0xbc000000, v63
	v_fmac_f32_e32 v62, 0xbc000000, v103
	v_fmamk_f32 v68, v103, 0xbc000000, v65
	v_fmac_f32_e32 v64, 0xbc000000, v103
	v_mul_f32_e32 v76, v64, v64
	v_mul_f32_e32 v78, v68, v68
	v_mul_f32_e32 v74, v62, v62
	v_mul_f32_e32 v66, v69, v69
	v_pk_add_f32 v[76:77], v[76:77], v[78:79]
	v_pk_add_f32 v[66:67], v[74:75], v[66:67]
	v_fmamk_f32 v59, v103, 0xbc000000, v59
	v_pk_add_f32 v[66:67], v[76:77], v[66:67]
	v_fmac_f32_e32 v58, 0xbc000000, v103
	v_fmamk_f32 v61, v103, 0xbc000000, v61
	v_fmac_f32_e32 v60, 0xbc000000, v103
	v_pk_add_f32 v[74:75], v[66:67], v[66:67] op_sel_hi:[0,1]
	v_pk_mul_f32 v[66:67], v[60:61], v[60:61]
	v_pk_mul_f32 v[76:77], v[58:59], v[58:59]
	v_fmac_f32_e32 v56, 0xbc000000, v103
	v_pk_mov_b32 v[78:79], v[76:77], v[66:67] op_sel:[1,0]
	v_mov_b32_e32 v77, v67
	v_pk_add_f32 v[66:67], v[78:79], v[76:77]
	v_fmamk_f32 v57, v103, 0xbc000000, v57
	v_pk_add_f32 v[76:77], v[66:67], v[66:67] op_sel_hi:[0,1]
	v_fmac_f32_e32 v54, 0xbc000000, v103
	v_mul_f32_e32 v66, v56, v56
	v_fmamk_f32 v55, v103, 0xbc000000, v55
	v_pk_fma_f32 v[78:79], v[56:57], v[56:57], v[66:67] op_sel_hi:[1,1,0]
	v_mul_f32_e32 v66, v54, v54
	v_pk_fma_f32 v[80:81], v[54:55], v[54:55], v[66:67] op_sel_hi:[1,1,0]
	v_fmamk_f32 v67, v103, 0xbc000000, v51
	v_fmac_f32_e32 v50, 0xbc000000, v103
	v_fmamk_f32 v66, v103, 0xbc000000, v53
	v_fmac_f32_e32 v52, 0xbc000000, v103
	v_mul_f32_e32 v78, v52, v52
	v_mul_f32_e32 v80, v66, v66
	v_mul_f32_e32 v76, v50, v50
	v_mul_f32_e32 v74, v67, v67
	v_pk_add_f32 v[78:79], v[78:79], v[80:81]
	v_pk_add_f32 v[74:75], v[76:77], v[74:75]
	v_mov_b32_e32 v95, v96
	v_pk_add_f32 v[74:75], v[78:79], v[74:75]
	v_lshlrev_b32_e32 v81, 16, v145
	v_add_f32_e32 v51, v74, v75
	v_mov_b32_e32 v53, v51
	s_nop 1
	v_permlane16_swap_b32 v53, v51
	s_nop 0
	v_lshlrev_b32_e32 v80, 16, v144
	v_lshlrev_b64 v[76:77], 12, v[146:147]
	v_lshl_add_u64 v[76:77], s[78:79], 0, v[76:77]
	v_lshl_add_u64 v[76:77], v[76:77], 0, s[0:1]
	s_waitcnt lgkmcnt(0)
	v_add_f32_e32 v51, v51, v53
	v_mov_b32_e32 v53, v51
	s_nop 1
	v_permlane32_swap_b32 v53, v51
	s_nop 0
	v_lshl_add_u64 v[76:77], v[76:77], 0, v[98:99]
	v_mov_b32_e32 v91, v92
	s_waitcnt lgkmcnt(0)
	v_add_f32_e32 v51, v51, v53
	v_fmamk_f32 v51, v51, 0x3c000000, v197
	v_mul_f32_e32 v53, 0x4f800000, v51
	v_cmp_gt_f32_e32 vcc, s34, v51
	s_nop 1
	v_cndmask_b32_e32 v51, v51, v53, vcc
	v_sqrt_f32_e32 v53, v51
	s_nop 0
	v_add_u32_e32 v63, -1, v53
	v_fma_f32 v65, -v63, v53, v51
	v_cmp_ge_f32_e64 s[74:75], 0, v65
	v_add_u32_e32 v65, 1, v53
	s_nop 0
	v_cndmask_b32_e64 v63, v53, v63, s[74:75]
	v_fma_f32 v53, -v65, v53, v51
	v_cmp_lt_f32_e64 s[74:75], 0, v53
	s_nop 1
	v_cndmask_b32_e64 v53, v63, v65, s[74:75]
	v_mul_f32_e32 v63, 0x37800000, v53
	v_cndmask_b32_e32 v53, v53, v63, vcc
	v_cmp_class_f32_e32 vcc, v51, v199
	s_nop 1
	v_cndmask_b32_e32 v51, v53, v51, vcc
	v_div_scale_f32 v53, s[34:35], v51, v51, 1.0
	v_rcp_f32_e32 v63, v53
	s_nop 0
	v_fma_f32 v65, -v53, v63, 1.0
	v_fmac_f32_e32 v63, v65, v63
	v_div_scale_f32 v65, vcc, 1.0, v51, 1.0
	v_mul_f32_e32 v74, v65, v63
	v_fma_f32 v75, -v53, v74, v65
	v_fmac_f32_e32 v74, v75, v63
	v_fma_f32 v53, -v53, v74, v65
	v_div_fmas_f32 v53, v53, v63, v74
	v_div_fixup_f32 v74, v53, v51, 1.0
	v_pk_mul_f32 v[78:79], v[94:95], v[74:75] op_sel_hi:[1,0]
	v_and_b32_e32 v95, 0xffff0000, v145
	v_pk_mul_f32 v[78:79], v[78:79], v[80:81]
	v_mov_b32_e32 v80, v72
	v_mov_b32_e32 v81, v70
	v_pk_mul_f32 v[80:81], v[80:81], v[74:75] op_sel_hi:[1,0]
	v_and_b32_e32 v94, 0xffff0000, v144
	v_pk_mul_f32 v[80:81], v[80:81], v[94:95]
	v_and_b32_sdwa v51, v79, v204 dst_sel:DWORD dst_unused:UNUSED_PAD src0_sel:WORD_1 src1_sel:DWORD
	v_and_b32_sdwa v63, v81, v204 dst_sel:DWORD dst_unused:UNUSED_PAD src0_sel:WORD_1 src1_sel:DWORD
	v_and_b32_sdwa v65, v80, v204 dst_sel:DWORD dst_unused:UNUSED_PAD src0_sel:WORD_1 src1_sel:DWORD
	v_and_b32_sdwa v53, v78, v204 dst_sel:DWORD dst_unused:UNUSED_PAD src0_sel:WORD_1 src1_sel:DWORD
	v_add3_u32 v63, v81, v63, s2
	v_add3_u32 v65, v80, v65, s2
	v_add3_u32 v53, v78, v53, s2
	v_add3_u32 v51, v79, v51, s2
	v_and_b32_e32 v63, 0xffff0000, v63
	v_and_b32_e32 v65, 0xffff0000, v65
	v_mov_b32_e32 v70, v73
	v_or_b32_sdwa v79, v63, v51 dst_sel:DWORD dst_unused:UNUSED_PAD src0_sel:DWORD src1_sel:WORD_1
	v_or_b32_sdwa v78, v65, v53 dst_sel:DWORD dst_unused:UNUSED_PAD src0_sel:DWORD src1_sel:WORD_1
	v_pk_mul_f32 v[70:71], v[70:71], v[74:75] op_sel_hi:[1,0]
	v_and_b32_e32 v73, 0xffff0000, v143
	v_and_b32_e32 v72, 0xffff0000, v142
	global_store_dwordx2 v[76:77], v[78:79], off offset:2048
	v_pk_mul_f32 v[78:79], v[90:91], v[74:75] op_sel_hi:[1,0]
	v_lshlrev_b32_e32 v81, 16, v143
	v_lshlrev_b32_e32 v80, 16, v142
	v_pk_mul_f32 v[70:71], v[70:71], v[72:73]
	v_pk_mul_f32 v[78:79], v[78:79], v[80:81]
	v_and_b32_sdwa v63, v71, v204 dst_sel:DWORD dst_unused:UNUSED_PAD src0_sel:WORD_1 src1_sel:DWORD
	v_and_b32_sdwa v65, v70, v204 dst_sel:DWORD dst_unused:UNUSED_PAD src0_sel:WORD_1 src1_sel:DWORD
	v_and_b32_sdwa v51, v79, v204 dst_sel:DWORD dst_unused:UNUSED_PAD src0_sel:WORD_1 src1_sel:DWORD
	v_and_b32_sdwa v53, v78, v204 dst_sel:DWORD dst_unused:UNUSED_PAD src0_sel:WORD_1 src1_sel:DWORD
	v_add3_u32 v63, v71, v63, s2
	v_add3_u32 v65, v70, v65, s2
	v_add3_u32 v53, v78, v53, s2
	v_add3_u32 v51, v79, v51, s2
	v_and_b32_e32 v63, 0xffff0000, v63
	v_and_b32_e32 v65, 0xffff0000, v65
	v_or_b32_sdwa v71, v63, v51 dst_sel:DWORD dst_unused:UNUSED_PAD src0_sel:DWORD src1_sel:WORD_1
	v_or_b32_sdwa v70, v65, v53 dst_sel:DWORD dst_unused:UNUSED_PAD src0_sel:DWORD src1_sel:WORD_1
	global_store_dwordx2 v[76:77], v[70:71], off offset:2080
	v_mov_b32_e32 v70, v86
	v_mov_b32_e32 v71, v88
	v_pk_mul_f32 v[70:71], v[70:71], v[74:75] op_sel_hi:[1,0]
	v_lshlrev_b32_e32 v73, 16, v141
	v_lshlrev_b32_e32 v72, 16, v140
	v_mov_b32_e32 v88, v87
	v_pk_mul_f32 v[70:71], v[70:71], v[72:73]
	v_pk_mul_f32 v[72:73], v[88:89], v[74:75] op_sel_hi:[1,0]
	v_and_b32_e32 v79, 0xffff0000, v141
	v_and_b32_e32 v78, 0xffff0000, v140
	v_pk_mul_f32 v[72:73], v[72:73], v[78:79]
	v_and_b32_sdwa v51, v71, v204 dst_sel:DWORD dst_unused:UNUSED_PAD src0_sel:WORD_1 src1_sel:DWORD
	v_and_b32_sdwa v63, v73, v204 dst_sel:DWORD dst_unused:UNUSED_PAD src0_sel:WORD_1 src1_sel:DWORD
	v_and_b32_sdwa v65, v72, v204 dst_sel:DWORD dst_unused:UNUSED_PAD src0_sel:WORD_1 src1_sel:DWORD
	v_and_b32_sdwa v53, v70, v204 dst_sel:DWORD dst_unused:UNUSED_PAD src0_sel:WORD_1 src1_sel:DWORD
	v_add3_u32 v63, v73, v63, s2
	v_add3_u32 v65, v72, v65, s2
	v_add3_u32 v53, v70, v53, s2
	v_add3_u32 v51, v71, v51, s2
	v_and_b32_e32 v63, 0xffff0000, v63
	v_and_b32_e32 v65, 0xffff0000, v65
	v_or_b32_sdwa v71, v63, v51 dst_sel:DWORD dst_unused:UNUSED_PAD src0_sel:DWORD src1_sel:WORD_1
	v_or_b32_sdwa v70, v65, v53 dst_sel:DWORD dst_unused:UNUSED_PAD src0_sel:DWORD src1_sel:WORD_1
	global_store_dwordx2 v[76:77], v[70:71], off offset:2112
	v_mov_b32_e32 v70, v82
	v_mov_b32_e32 v71, v84
	v_pk_mul_f32 v[70:71], v[70:71], v[74:75] op_sel_hi:[1,0]
	v_lshlrev_b32_e32 v73, 16, v139
	v_lshlrev_b32_e32 v72, 16, v138
	v_mov_b32_e32 v84, v83
	v_pk_mul_f32 v[70:71], v[70:71], v[72:73]
	v_pk_mul_f32 v[72:73], v[84:85], v[74:75] op_sel_hi:[1,0]
	v_and_b32_e32 v79, 0xffff0000, v139
	v_and_b32_e32 v78, 0xffff0000, v138
	v_pk_mul_f32 v[72:73], v[72:73], v[78:79]
	v_and_b32_sdwa v53, v70, v204 dst_sel:DWORD dst_unused:UNUSED_PAD src0_sel:WORD_1 src1_sel:DWORD
	v_and_b32_sdwa v65, v72, v204 dst_sel:DWORD dst_unused:UNUSED_PAD src0_sel:WORD_1 src1_sel:DWORD
	v_and_b32_sdwa v63, v73, v204 dst_sel:DWORD dst_unused:UNUSED_PAD src0_sel:WORD_1 src1_sel:DWORD
	v_add3_u32 v65, v72, v65, s2
	v_and_b32_sdwa v51, v71, v204 dst_sel:DWORD dst_unused:UNUSED_PAD src0_sel:WORD_1 src1_sel:DWORD
	v_add3_u32 v53, v70, v53, s2
	v_add3_u32 v63, v73, v63, s2
	v_and_b32_e32 v65, 0xffff0000, v65
	v_add3_u32 v51, v71, v51, s2
	v_and_b32_e32 v63, 0xffff0000, v63
	v_or_b32_sdwa v70, v65, v53 dst_sel:DWORD dst_unused:UNUSED_PAD src0_sel:DWORD src1_sel:WORD_1
	v_mov_b32_e32 v65, v62
	v_or_b32_sdwa v71, v63, v51 dst_sel:DWORD dst_unused:UNUSED_PAD src0_sel:DWORD src1_sel:WORD_1
	v_pk_mul_f32 v[62:63], v[64:65], v[74:75] op_sel_hi:[1,0]
	v_lshlrev_b32_e32 v65, 16, v137
	v_lshlrev_b32_e32 v64, 16, v136
	v_pk_mul_f32 v[62:63], v[62:63], v[64:65]
	v_pk_mul_f32 v[64:65], v[68:69], v[74:75] op_sel_hi:[1,0]
	v_and_b32_e32 v69, 0xffff0000, v137
	v_and_b32_e32 v68, 0xffff0000, v136
	v_pk_mul_f32 v[64:65], v[64:65], v[68:69]
	v_and_b32_sdwa v51, v63, v204 dst_sel:DWORD dst_unused:UNUSED_PAD src0_sel:WORD_1 src1_sel:DWORD
	v_and_b32_sdwa v53, v62, v204 dst_sel:DWORD dst_unused:UNUSED_PAD src0_sel:WORD_1 src1_sel:DWORD
	v_add3_u32 v53, v62, v53, s2
	v_add3_u32 v51, v63, v51, s2
	v_and_b32_sdwa v62, v65, v204 dst_sel:DWORD dst_unused:UNUSED_PAD src0_sel:WORD_1 src1_sel:DWORD
	v_and_b32_sdwa v63, v64, v204 dst_sel:DWORD dst_unused:UNUSED_PAD src0_sel:WORD_1 src1_sel:DWORD
	v_add3_u32 v62, v65, v62, s2
	v_add3_u32 v63, v64, v63, s2
	v_and_b32_e32 v62, 0xffff0000, v62
	v_and_b32_e32 v64, 0xffff0000, v63
	v_or_b32_sdwa v63, v62, v51 dst_sel:DWORD dst_unused:UNUSED_PAD src0_sel:DWORD src1_sel:WORD_1
	v_or_b32_sdwa v62, v64, v53 dst_sel:DWORD dst_unused:UNUSED_PAD src0_sel:DWORD src1_sel:WORD_1
	global_store_dwordx2 v[76:77], v[62:63], off offset:2176
	v_mov_b32_e32 v63, v60
	v_mov_b32_e32 v60, v59
	v_mov_b32_e32 v62, v58
	v_pk_mul_f32 v[58:59], v[60:61], v[74:75] op_sel_hi:[1,0]
	v_and_b32_e32 v61, 0xffff0000, v135
	v_and_b32_e32 v60, 0xffff0000, v134
	v_pk_mul_f32 v[62:63], v[62:63], v[74:75] op_sel_hi:[1,0]
	v_lshlrev_b32_e32 v65, 16, v135
	v_lshlrev_b32_e32 v64, 16, v134
	v_pk_mul_f32 v[58:59], v[58:59], v[60:61]
	v_pk_mul_f32 v[62:63], v[62:63], v[64:65]
	v_and_b32_sdwa v60, v59, v204 dst_sel:DWORD dst_unused:UNUSED_PAD src0_sel:WORD_1 src1_sel:DWORD
	v_and_b32_sdwa v61, v58, v204 dst_sel:DWORD dst_unused:UNUSED_PAD src0_sel:WORD_1 src1_sel:DWORD
	v_and_b32_sdwa v51, v63, v204 dst_sel:DWORD dst_unused:UNUSED_PAD src0_sel:WORD_1 src1_sel:DWORD
	v_and_b32_sdwa v53, v62, v204 dst_sel:DWORD dst_unused:UNUSED_PAD src0_sel:WORD_1 src1_sel:DWORD
	v_add3_u32 v59, v59, v60, s2
	v_add3_u32 v58, v58, v61, s2
	v_add3_u32 v53, v62, v53, s2
	v_add3_u32 v51, v63, v51, s2
	v_and_b32_e32 v59, 0xffff0000, v59
	v_and_b32_e32 v58, 0xffff0000, v58
	v_or_b32_sdwa v59, v59, v51 dst_sel:DWORD dst_unused:UNUSED_PAD src0_sel:DWORD src1_sel:WORD_1
	v_or_b32_sdwa v58, v58, v53 dst_sel:DWORD dst_unused:UNUSED_PAD src0_sel:DWORD src1_sel:WORD_1
	global_store_dwordx2 v[76:77], v[58:59], off offset:2208
	v_mov_b32_e32 v59, v54
	v_mov_b32_e32 v54, v57
	v_mov_b32_e32 v58, v56
	v_pk_mul_f32 v[54:55], v[54:55], v[74:75] op_sel_hi:[1,0]
	v_and_b32_e32 v57, 0xffff0000, v133
	v_and_b32_e32 v56, 0xffff0000, v132
	v_pk_mul_f32 v[58:59], v[58:59], v[74:75] op_sel_hi:[1,0]
	v_lshlrev_b32_e32 v61, 16, v133
	v_lshlrev_b32_e32 v60, 16, v132
	v_pk_mul_f32 v[54:55], v[54:55], v[56:57]
	v_pk_mul_f32 v[58:59], v[58:59], v[60:61]
	v_and_b32_sdwa v57, v54, v204 dst_sel:DWORD dst_unused:UNUSED_PAD src0_sel:WORD_1 src1_sel:DWORD
	v_and_b32_sdwa v53, v58, v204 dst_sel:DWORD dst_unused:UNUSED_PAD src0_sel:WORD_1 src1_sel:DWORD
	v_and_b32_sdwa v56, v55, v204 dst_sel:DWORD dst_unused:UNUSED_PAD src0_sel:WORD_1 src1_sel:DWORD
	v_add3_u32 v54, v54, v57, s2
	v_and_b32_sdwa v51, v59, v204 dst_sel:DWORD dst_unused:UNUSED_PAD src0_sel:WORD_1 src1_sel:DWORD
	v_add3_u32 v53, v58, v53, s2
	v_add3_u32 v55, v55, v56, s2
	v_and_b32_e32 v54, 0xffff0000, v54
	v_add3_u32 v51, v59, v51, s2
	v_and_b32_e32 v55, 0xffff0000, v55
	v_or_b32_sdwa v54, v54, v53 dst_sel:DWORD dst_unused:UNUSED_PAD src0_sel:DWORD src1_sel:WORD_1
	v_mov_b32_e32 v53, v50
	v_or_b32_sdwa v55, v55, v51 dst_sel:DWORD dst_unused:UNUSED_PAD src0_sel:DWORD src1_sel:WORD_1
	v_pk_mul_f32 v[50:51], v[52:53], v[74:75] op_sel_hi:[1,0]
	v_lshlrev_b32_e32 v53, 16, v131
	v_lshlrev_b32_e32 v52, 16, v130
	global_store_dwordx2 v[76:77], v[54:55], off offset:2240
	v_pk_mul_f32 v[50:51], v[50:51], v[52:53]
	v_pk_mul_f32 v[52:53], v[66:67], v[74:75] op_sel_hi:[1,0]
	v_and_b32_e32 v55, 0xffff0000, v131
	v_and_b32_e32 v54, 0xffff0000, v130
	v_pk_mul_f32 v[52:53], v[52:53], v[54:55]
	v_and_b32_sdwa v54, v51, v204 dst_sel:DWORD dst_unused:UNUSED_PAD src0_sel:WORD_1 src1_sel:DWORD
	v_and_b32_sdwa v55, v50, v204 dst_sel:DWORD dst_unused:UNUSED_PAD src0_sel:WORD_1 src1_sel:DWORD
	v_add3_u32 v50, v50, v55, s2
	v_add3_u32 v51, v51, v54, s2
	v_and_b32_sdwa v54, v53, v204 dst_sel:DWORD dst_unused:UNUSED_PAD src0_sel:WORD_1 src1_sel:DWORD
	v_and_b32_sdwa v55, v52, v204 dst_sel:DWORD dst_unused:UNUSED_PAD src0_sel:WORD_1 src1_sel:DWORD
	v_add3_u32 v53, v53, v54, s2
	v_add3_u32 v52, v52, v55, s2
	v_and_b32_e32 v53, 0xffff0000, v53
	v_and_b32_e32 v52, 0xffff0000, v52
	v_or_b32_sdwa v51, v53, v51 dst_sel:DWORD dst_unused:UNUSED_PAD src0_sel:DWORD src1_sel:WORD_1
	v_or_b32_sdwa v50, v52, v50 dst_sel:DWORD dst_unused:UNUSED_PAD src0_sel:DWORD src1_sel:WORD_1
	global_store_dwordx2 v[76:77], v[50:51], off offset:2272
	s_waitcnt vmcnt(7)
	v_mov_b64_e32 v[64:65], v[36:37]
	v_mov_b64_e32 v[60:61], v[40:41]
	v_mov_b64_e32 v[56:57], v[44:45]
	v_mov_b64_e32 v[52:53], v[48:49]
	s_andn2_b64 vcc, exec, s[30:31]
	v_mov_b64_e32 v[62:63], v[34:35]
	v_mov_b64_e32 v[58:59], v[38:39]
	v_mov_b64_e32 v[54:55], v[42:43]
	v_mov_b64_e32 v[50:51], v[46:47]
	global_store_dwordx2 v[76:77], v[70:71], off offset:2144
	s_barrier
	s_cbranch_vccnz .LBB0_656
	v_readlane_b32 s54, v252, 54
	v_readlane_b32 s80, v252, 45
	v_readlane_b32 s90, v252, 43
	v_readlane_b32 s95, v252, 53
	v_readlane_b32 s55, v252, 55
	v_readlane_b32 s81, v252, 46
	v_readlane_b32 s91, v252, 44
